# gate|up: both per-unit alignment barriers moved into the SwiGLU epilogue (leading half after group 2, trailing half after group 6)
# baseline (speedup 1.0000x reference)
; __device__ __forceinline__ unsigned cvt_pk_bf16(float lo, float hi) { const f32x2_t v = {lo, hi}; const bf16x2_t b = __builtin_convertvector(v, bf16x2_t); return __builtin_bit_cast(unsigned, b); }
;     __device__ __forceinline__ void operator()(const f32x4 (&acc)[2][2][4][2], const Unit& u, int wr, int wc, int fr, int fq, int ui) const {
;     ...
;                 for (int n = 0; n < 2; ++n)
; #pragma unroll
;                     for (int i = 0; i < 4; ++i) { g[n * 4 + i] = fmaf(acc[ai][0][m][n][i], r, bg[n][i]); v[n * 4 + i] = fmaf(acc[ai][1][m][n][i], r, bu[n][i]); }
; #pragma unroll
;                 for (int i = 0; i < 8; ++i) e[i] = __builtin_amdgcn_exp2f(g[i] * (-LOG2E));
; #pragma unroll
;                 for (int i = 0; i < 8; ++i) e[i] = __builtin_amdgcn_rcpf(1.0f + e[i]);
; #pragma unroll
;                 for (int i = 0; i < 8; ++i) e[i] = (g[i] * e[i]) * v[i];
;                 u32x4 w; w.x = cvt_pk_bf16(e[0], e[1]); w.y = cvt_pk_bf16(e[2], e[3]); w.z = cvt_pk_bf16(e[4], e[5]); w.w = cvt_pk_bf16(e[6], e[7]);
;                 *(u32x4*)(act + ((size_t)((row >> 8) * (F / 64) + (jcol >> 6)) * 256 + (row & 255)) * 64 + (jcol & 63)) = w;
.Lgu_bar1:
	v_pk_fma_f32 v[108:109], v[108:109], v[176:177], v[96:97] op_sel_hi:[1,0,1]
	v_pk_fma_f32 v[110:111], v[110:111], v[176:177], v[98:99] op_sel_hi:[1,0,1]
	v_pk_fma_f32 v[92:93], v[92:93], v[176:177], v[80:81] op_sel_hi:[1,0,1]
	v_pk_fma_f32 v[94:95], v[94:95], v[176:177], v[82:83] op_sel_hi:[1,0,1]
	v_pk_mul_f32 v[198:199], v[108:109], v[222:223] op_sel_hi:[1,0]
	v_pk_mul_f32 v[200:201], v[110:111], v[222:223] op_sel_hi:[1,0]
	v_pk_mul_f32 v[202:203], v[92:93], v[222:223] op_sel_hi:[1,0]
	v_pk_mul_f32 v[204:205], v[94:95], v[222:223] op_sel_hi:[1,0]
	v_pk_fma_f32 v[104:105], v[104:105], v[176:177], v[100:101] op_sel_hi:[1,0,1]
	v_pk_fma_f32 v[106:107], v[106:107], v[176:177], v[102:103] op_sel_hi:[1,0,1]
	v_pk_fma_f32 v[88:89], v[88:89], v[176:177], v[84:85] op_sel_hi:[1,0,1]
	v_pk_fma_f32 v[90:91], v[90:91], v[176:177], v[86:87] op_sel_hi:[1,0,1]
	v_exp_f32_e32 v198, v198
	v_exp_f32_e32 v199, v199
	v_exp_f32_e32 v200, v200
	v_exp_f32_e32 v201, v201
	v_exp_f32_e32 v202, v202
	v_exp_f32_e32 v203, v203
	v_exp_f32_e32 v204, v204
	v_exp_f32_e32 v205, v205
	v_pk_add_f32 v[198:199], v[198:199], v[224:225] op_sel_hi:[1,0]
	v_pk_add_f32 v[200:201], v[200:201], v[224:225] op_sel_hi:[1,0]
	v_pk_add_f32 v[202:203], v[202:203], v[224:225] op_sel_hi:[1,0]
	v_pk_add_f32 v[204:205], v[204:205], v[224:225] op_sel_hi:[1,0]
	v_rcp_f32_e32 v198, v198
	v_rcp_f32_e32 v199, v199
	v_rcp_f32_e32 v200, v200
	v_rcp_f32_e32 v201, v201
	v_rcp_f32_e32 v202, v202
	v_rcp_f32_e32 v203, v203
	v_rcp_f32_e32 v204, v204
	v_rcp_f32_e32 v205, v205
	v_pk_mul_f32 v[108:109], v[108:109], v[198:199]
	v_pk_mul_f32 v[110:111], v[110:111], v[200:201]
	v_pk_mul_f32 v[92:93], v[92:93], v[202:203]
	v_pk_mul_f32 v[94:95], v[94:95], v[204:205]
	v_pk_mul_f32 v[108:109], v[104:105], v[108:109]
	v_pk_mul_f32 v[110:111], v[106:107], v[110:111]
	v_pk_mul_f32 v[92:93], v[88:89], v[92:93]
	v_pk_mul_f32 v[94:95], v[90:91], v[94:95]
	v_cvt_pk_bf16_f32 v206, v108, v109
	v_cvt_pk_bf16_f32 v207, v110, v111
	v_cvt_pk_bf16_f32 v208, v92, v93
	v_cvt_pk_bf16_f32 v209, v94, v95
	global_store_dwordx4 v[214:215], v[206:209], off
	v_pk_fma_f32 v[76:77], v[76:77], v[176:177], v[96:97] op_sel:[0,1,0]
	v_pk_fma_f32 v[78:79], v[78:79], v[176:177], v[98:99] op_sel:[0,1,0]
	v_pk_fma_f32 v[68:69], v[68:69], v[176:177], v[80:81] op_sel:[0,1,0]
	v_pk_fma_f32 v[70:71], v[70:71], v[176:177], v[82:83] op_sel:[0,1,0]
	v_pk_mul_f32 v[198:199], v[76:77], v[222:223] op_sel_hi:[1,0]
	v_pk_mul_f32 v[200:201], v[78:79], v[222:223] op_sel_hi:[1,0]
	v_pk_mul_f32 v[202:203], v[68:69], v[222:223] op_sel_hi:[1,0]
	v_pk_mul_f32 v[204:205], v[70:71], v[222:223] op_sel_hi:[1,0]
	v_pk_fma_f32 v[72:73], v[72:73], v[176:177], v[100:101] op_sel:[0,1,0]
	v_pk_fma_f32 v[74:75], v[74:75], v[176:177], v[102:103] op_sel:[0,1,0]
	v_pk_fma_f32 v[64:65], v[64:65], v[176:177], v[84:85] op_sel:[0,1,0]
	v_pk_fma_f32 v[66:67], v[66:67], v[176:177], v[86:87] op_sel:[0,1,0]
	v_exp_f32_e32 v198, v198
	v_exp_f32_e32 v199, v199
	v_exp_f32_e32 v200, v200
	v_exp_f32_e32 v201, v201
	v_exp_f32_e32 v202, v202
	v_exp_f32_e32 v203, v203
	v_exp_f32_e32 v204, v204
	v_exp_f32_e32 v205, v205
	v_pk_add_f32 v[198:199], v[198:199], v[224:225] op_sel_hi:[1,0]
	v_pk_add_f32 v[200:201], v[200:201], v[224:225] op_sel_hi:[1,0]
	v_pk_add_f32 v[202:203], v[202:203], v[224:225] op_sel_hi:[1,0]
	v_pk_add_f32 v[204:205], v[204:205], v[224:225] op_sel_hi:[1,0]
	v_rcp_f32_e32 v198, v198
	v_rcp_f32_e32 v199, v199
	v_rcp_f32_e32 v200, v200
	v_rcp_f32_e32 v201, v201
	v_rcp_f32_e32 v202, v202
	v_rcp_f32_e32 v203, v203
	v_rcp_f32_e32 v204, v204
	v_rcp_f32_e32 v205, v205
	v_pk_mul_f32 v[76:77], v[76:77], v[198:199]
	v_pk_mul_f32 v[78:79], v[78:79], v[200:201]
	v_pk_mul_f32 v[68:69], v[68:69], v[202:203]
	v_pk_mul_f32 v[70:71], v[70:71], v[204:205]
	v_pk_mul_f32 v[76:77], v[72:73], v[76:77]
	v_pk_mul_f32 v[78:79], v[74:75], v[78:79]
	v_pk_mul_f32 v[68:69], v[64:65], v[68:69]
	v_pk_mul_f32 v[70:71], v[66:67], v[70:71]
	v_cvt_pk_bf16_f32 v210, v76, v77
	v_cvt_pk_bf16_f32 v211, v78, v79
	v_cvt_pk_bf16_f32 v212, v68, v69
	v_cvt_pk_bf16_f32 v213, v70, v71
	global_store_dwordx4 v[214:215], v[210:213], off offset:2048
	v_pk_fma_f32 v[60:61], v[60:61], v[164:165], v[96:97] op_sel_hi:[1,0,1]
	v_pk_fma_f32 v[62:63], v[62:63], v[164:165], v[98:99] op_sel_hi:[1,0,1]
	v_pk_fma_f32 v[52:53], v[52:53], v[164:165], v[80:81] op_sel_hi:[1,0,1]
	v_pk_fma_f32 v[54:55], v[54:55], v[164:165], v[82:83] op_sel_hi:[1,0,1]
	v_pk_mul_f32 v[198:199], v[60:61], v[222:223] op_sel_hi:[1,0]
	v_pk_mul_f32 v[200:201], v[62:63], v[222:223] op_sel_hi:[1,0]
	v_pk_mul_f32 v[202:203], v[52:53], v[222:223] op_sel_hi:[1,0]
	v_pk_mul_f32 v[204:205], v[54:55], v[222:223] op_sel_hi:[1,0]
	v_pk_fma_f32 v[56:57], v[56:57], v[164:165], v[100:101] op_sel_hi:[1,0,1]
	v_pk_fma_f32 v[58:59], v[58:59], v[164:165], v[102:103] op_sel_hi:[1,0,1]
	v_pk_fma_f32 v[48:49], v[48:49], v[164:165], v[84:85] op_sel_hi:[1,0,1]
	v_pk_fma_f32 v[50:51], v[50:51], v[164:165], v[86:87] op_sel_hi:[1,0,1]
	v_exp_f32_e32 v198, v198
	v_exp_f32_e32 v199, v199
	v_exp_f32_e32 v200, v200
	v_exp_f32_e32 v201, v201
	v_exp_f32_e32 v202, v202
	v_exp_f32_e32 v203, v203
	v_exp_f32_e32 v204, v204
	v_exp_f32_e32 v205, v205
	v_pk_add_f32 v[198:199], v[198:199], v[224:225] op_sel_hi:[1,0]
	v_pk_add_f32 v[200:201], v[200:201], v[224:225] op_sel_hi:[1,0]
	v_pk_add_f32 v[202:203], v[202:203], v[224:225] op_sel_hi:[1,0]
	v_pk_add_f32 v[204:205], v[204:205], v[224:225] op_sel_hi:[1,0]
	v_rcp_f32_e32 v198, v198
	v_rcp_f32_e32 v199, v199
	v_rcp_f32_e32 v200, v200
	v_rcp_f32_e32 v201, v201
	v_rcp_f32_e32 v202, v202
	v_rcp_f32_e32 v203, v203
	v_rcp_f32_e32 v204, v204
; __device__ __forceinline__ unsigned cvt_pk_bf16(float lo, float hi) { const f32x2_t v = {lo, hi}; const bf16x2_t b = __builtin_convertvector(v, bf16x2_t); return __builtin_bit_cast(unsigned, b); }
; #define PG8_BAR __builtin_amdgcn_s_barrier()
;     __device__ __forceinline__ void operator()(const f32x4 (&acc)[2][2][4][2], const Unit& u, int wr, int wc, int fr, int fq, int ui) const {
;     ...
;                 for (int n = 0; n < 2; ++n)
; #pragma unroll
;                     for (int i = 0; i < 4; ++i) { g[n * 4 + i] = fmaf(acc[ai][0][m][n][i], r, bg[n][i]); v[n * 4 + i] = fmaf(acc[ai][1][m][n][i], r, bu[n][i]); }
; #pragma unroll
;                 for (int i = 0; i < 8; ++i) e[i] = __builtin_amdgcn_exp2f(g[i] * (-LOG2E));
; #pragma unroll
;                 for (int i = 0; i < 8; ++i) e[i] = __builtin_amdgcn_rcpf(1.0f + e[i]);
; #pragma unroll
;                 for (int i = 0; i < 8; ++i) e[i] = (g[i] * e[i]) * v[i];
;                 u32x4 w; w.x = cvt_pk_bf16(e[0], e[1]); w.y = cvt_pk_bf16(e[2], e[3]); w.z = cvt_pk_bf16(e[4], e[5]); w.w = cvt_pk_bf16(e[6], e[7]);
;                 *(u32x4*)(act + ((size_t)((row >> 8) * (F / 64) + (jcol >> 6)) * 256 + (row & 255)) * 64 + (jcol & 63)) = w;
; template <class Epi, class Sched, bool ALIGN_EPI>
; __device__ __forceinline__ void gemm_phase(PG8_LAS unsigned char* lds, const Gemm g, const Sched& S, const Epi& E, const int tid) {
;     ...
;         }
;         if constexpr (ALIGN_EPI) { if (wr == 0) PG8_BAR; }
;         E(acc, cur, wr, wc, fr, fq, ui); S.done(cur);
;         if (!has_next) break;
; #pragma unroll
;         for (int a = 0; a < 2; ++a)
; #pragma unroll
;             for (int b = 0; b < 2; ++b)
; #pragma unroll
;                 for (int m = 0; m < 4; ++m)
; #pragma unroll
;                     for (int n = 0; n < 2; ++n) acc[a][b][m][n] = (f32x4){0.f, 0.f, 0.f, 0.f};
;         cur = nxt; cA = nA; cB = nB; ++ui;
;         if constexpr (ALIGN_EPI) { if (wr == 1) PG8_BAR; }
	v_rcp_f32_e32 v205, v205
	v_pk_mul_f32 v[60:61], v[60:61], v[198:199]
	v_pk_mul_f32 v[62:63], v[62:63], v[200:201]
	v_pk_mul_f32 v[52:53], v[52:53], v[202:203]
	v_pk_mul_f32 v[54:55], v[54:55], v[204:205]
	v_pk_mul_f32 v[60:61], v[56:57], v[60:61]
	v_pk_mul_f32 v[62:63], v[58:59], v[62:63]
	v_pk_mul_f32 v[52:53], v[48:49], v[52:53]
	v_pk_mul_f32 v[54:55], v[50:51], v[54:55]
	v_cvt_pk_bf16_f32 v206, v60, v61
	v_cvt_pk_bf16_f32 v207, v62, v63
	v_cvt_pk_bf16_f32 v208, v52, v53
	v_cvt_pk_bf16_f32 v209, v54, v55
	global_store_dwordx4 v[216:217], v[206:209], off offset:-4096
	v_pk_fma_f32 v[44:45], v[44:45], v[164:165], v[96:97] op_sel:[0,1,0]
	v_pk_fma_f32 v[46:47], v[46:47], v[164:165], v[98:99] op_sel:[0,1,0]
	v_pk_fma_f32 v[36:37], v[36:37], v[164:165], v[80:81] op_sel:[0,1,0]
	v_pk_fma_f32 v[38:39], v[38:39], v[164:165], v[82:83] op_sel:[0,1,0]
	v_pk_mul_f32 v[198:199], v[44:45], v[222:223] op_sel_hi:[1,0]
	v_pk_mul_f32 v[200:201], v[46:47], v[222:223] op_sel_hi:[1,0]
	v_pk_mul_f32 v[202:203], v[36:37], v[222:223] op_sel_hi:[1,0]
	v_pk_mul_f32 v[204:205], v[38:39], v[222:223] op_sel_hi:[1,0]
	v_pk_fma_f32 v[40:41], v[40:41], v[164:165], v[100:101] op_sel:[0,1,0]
	v_pk_fma_f32 v[42:43], v[42:43], v[164:165], v[102:103] op_sel:[0,1,0]
	v_pk_fma_f32 v[32:33], v[32:33], v[164:165], v[84:85] op_sel:[0,1,0]
	v_pk_fma_f32 v[34:35], v[34:35], v[164:165], v[86:87] op_sel:[0,1,0]
	v_exp_f32_e32 v198, v198
	v_exp_f32_e32 v199, v199
	v_exp_f32_e32 v200, v200
	v_exp_f32_e32 v201, v201
	v_exp_f32_e32 v202, v202
	v_exp_f32_e32 v203, v203
	v_exp_f32_e32 v204, v204
	v_exp_f32_e32 v205, v205
	v_pk_add_f32 v[198:199], v[198:199], v[224:225] op_sel_hi:[1,0]
	v_pk_add_f32 v[200:201], v[200:201], v[224:225] op_sel_hi:[1,0]
	v_pk_add_f32 v[202:203], v[202:203], v[224:225] op_sel_hi:[1,0]
	v_pk_add_f32 v[204:205], v[204:205], v[224:225] op_sel_hi:[1,0]
	v_rcp_f32_e32 v198, v198
	v_rcp_f32_e32 v199, v199
	v_rcp_f32_e32 v200, v200
	v_rcp_f32_e32 v201, v201
	v_rcp_f32_e32 v202, v202
	v_rcp_f32_e32 v203, v203
	v_rcp_f32_e32 v204, v204
	v_rcp_f32_e32 v205, v205
	v_pk_mul_f32 v[44:45], v[44:45], v[198:199]
	v_pk_mul_f32 v[46:47], v[46:47], v[200:201]
	v_pk_mul_f32 v[36:37], v[36:37], v[202:203]
	v_pk_mul_f32 v[38:39], v[38:39], v[204:205]
	v_pk_mul_f32 v[44:45], v[40:41], v[44:45]
	v_pk_mul_f32 v[46:47], v[42:43], v[46:47]
	v_pk_mul_f32 v[36:37], v[32:33], v[36:37]
	v_pk_mul_f32 v[38:39], v[34:35], v[38:39]
	v_cvt_pk_bf16_f32 v210, v44, v45
	v_cvt_pk_bf16_f32 v211, v46, v47
	v_cvt_pk_bf16_f32 v212, v36, v37
	v_cvt_pk_bf16_f32 v213, v38, v39
	global_store_dwordx4 v[216:217], v[210:213], off offset:-2048
	s_and_b64 vcc, s[2:3], s[4:5]
	s_and_b64 vcc, exec, vcc
	s_cbranch_vccz .Lgu_bar2
	s_barrier
.Lgu_bar2:
	v_pk_fma_f32 v[28:29], v[28:29], v[162:163], v[96:97] op_sel_hi:[1,0,1]
	v_pk_fma_f32 v[30:31], v[30:31], v[162:163], v[98:99] op_sel_hi:[1,0,1]
	v_pk_fma_f32 v[20:21], v[20:21], v[162:163], v[80:81] op_sel_hi:[1,0,1]
	v_pk_fma_f32 v[22:23], v[22:23], v[162:163], v[82:83] op_sel_hi:[1,0,1]
	v_pk_mul_f32 v[198:199], v[28:29], v[222:223] op_sel_hi:[1,0]
	v_pk_mul_f32 v[200:201], v[30:31], v[222:223] op_sel_hi:[1,0]
	v_pk_mul_f32 v[202:203], v[20:21], v[222:223] op_sel_hi:[1,0]
	v_pk_mul_f32 v[204:205], v[22:23], v[222:223] op_sel_hi:[1,0]
	v_pk_fma_f32 v[24:25], v[24:25], v[162:163], v[100:101] op_sel_hi:[1,0,1]
	v_pk_fma_f32 v[26:27], v[26:27], v[162:163], v[102:103] op_sel_hi:[1,0,1]
	v_pk_fma_f32 v[16:17], v[16:17], v[162:163], v[84:85] op_sel_hi:[1,0,1]
	v_pk_fma_f32 v[18:19], v[18:19], v[162:163], v[86:87] op_sel_hi:[1,0,1]
	v_exp_f32_e32 v198, v198
	v_exp_f32_e32 v199, v199
	v_exp_f32_e32 v200, v200
	v_exp_f32_e32 v201, v201
	v_exp_f32_e32 v202, v202
	v_exp_f32_e32 v203, v203
	v_exp_f32_e32 v204, v204
	v_exp_f32_e32 v205, v205
	v_pk_add_f32 v[198:199], v[198:199], v[224:225] op_sel_hi:[1,0]
	v_pk_add_f32 v[200:201], v[200:201], v[224:225] op_sel_hi:[1,0]
	v_pk_add_f32 v[202:203], v[202:203], v[224:225] op_sel_hi:[1,0]
	v_pk_add_f32 v[204:205], v[204:205], v[224:225] op_sel_hi:[1,0]
	v_rcp_f32_e32 v198, v198
	v_rcp_f32_e32 v199, v199
	v_rcp_f32_e32 v200, v200
	v_rcp_f32_e32 v201, v201
	v_rcp_f32_e32 v202, v202
	v_rcp_f32_e32 v203, v203
	v_rcp_f32_e32 v204, v204
	v_rcp_f32_e32 v205, v205
	v_pk_mul_f32 v[28:29], v[28:29], v[198:199]
	v_pk_mul_f32 v[30:31], v[30:31], v[200:201]
	v_pk_mul_f32 v[20:21], v[20:21], v[202:203]
	v_pk_mul_f32 v[22:23], v[22:23], v[204:205]
	v_pk_mul_f32 v[28:29], v[24:25], v[28:29]
	v_pk_mul_f32 v[30:31], v[26:27], v[30:31]
	v_pk_mul_f32 v[20:21], v[16:17], v[20:21]
	v_pk_mul_f32 v[22:23], v[18:19], v[22:23]
	v_cvt_pk_bf16_f32 v206, v28, v29
	v_cvt_pk_bf16_f32 v207, v30, v31
	v_cvt_pk_bf16_f32 v208, v20, v21
	v_cvt_pk_bf16_f32 v209, v22, v23
	global_store_dwordx4 v[216:217], v[206:209], off
	v_pk_fma_f32 v[12:13], v[12:13], v[162:163], v[96:97] op_sel:[0,1,0]
	v_pk_fma_f32 v[14:15], v[14:15], v[162:163], v[98:99] op_sel:[0,1,0]
	v_pk_fma_f32 v[4:5], v[4:5], v[162:163], v[80:81] op_sel:[0,1,0]
	v_pk_fma_f32 v[6:7], v[6:7], v[162:163], v[82:83] op_sel:[0,1,0]
	v_pk_mul_f32 v[198:199], v[12:13], v[222:223] op_sel_hi:[1,0]
	v_pk_mul_f32 v[200:201], v[14:15], v[222:223] op_sel_hi:[1,0]
	v_pk_mul_f32 v[202:203], v[4:5], v[222:223] op_sel_hi:[1,0]
	v_pk_mul_f32 v[204:205], v[6:7], v[222:223] op_sel_hi:[1,0]
	v_pk_fma_f32 v[8:9], v[8:9], v[162:163], v[100:101] op_sel:[0,1,0]
	v_pk_fma_f32 v[10:11], v[10:11], v[162:163], v[102:103] op_sel:[0,1,0]
	v_pk_fma_f32 v[0:1], v[0:1], v[162:163], v[84:85] op_sel:[0,1,0]
	v_pk_fma_f32 v[2:3], v[2:3], v[162:163], v[86:87] op_sel:[0,1,0]
	v_exp_f32_e32 v198, v198
	v_exp_f32_e32 v199, v199
	v_exp_f32_e32 v200, v200
	v_exp_f32_e32 v201, v201
	v_exp_f32_e32 v202, v202
	v_exp_f32_e32 v203, v203
	v_exp_f32_e32 v204, v204
	v_exp_f32_e32 v205, v205
	v_pk_add_f32 v[198:199], v[198:199], v[224:225] op_sel_hi:[1,0]
	v_pk_add_f32 v[200:201], v[200:201], v[224:225] op_sel_hi:[1,0]
	v_pk_add_f32 v[202:203], v[202:203], v[224:225] op_sel_hi:[1,0]
	v_pk_add_f32 v[204:205], v[204:205], v[224:225] op_sel_hi:[1,0]
	v_rcp_f32_e32 v198, v198
	v_rcp_f32_e32 v199, v199
	v_rcp_f32_e32 v200, v200
	v_rcp_f32_e32 v201, v201
	v_rcp_f32_e32 v202, v202
	v_rcp_f32_e32 v203, v203
	v_rcp_f32_e32 v204, v204
	v_rcp_f32_e32 v205, v205
	v_pk_mul_f32 v[12:13], v[12:13], v[198:199]
	v_pk_mul_f32 v[14:15], v[14:15], v[200:201]
	v_pk_mul_f32 v[4:5], v[4:5], v[202:203]
	v_pk_mul_f32 v[6:7], v[6:7], v[204:205]
	v_pk_mul_f32 v[12:13], v[8:9], v[12:13]
	v_pk_mul_f32 v[14:15], v[10:11], v[14:15]
	v_pk_mul_f32 v[4:5], v[0:1], v[4:5]
	v_pk_mul_f32 v[6:7], v[2:3], v[6:7]
	v_cvt_pk_bf16_f32 v210, v12, v13
	v_cvt_pk_bf16_f32 v211, v14, v15
	v_cvt_pk_bf16_f32 v212, v4, v5
	v_cvt_pk_bf16_f32 v213, v6, v7
	global_store_dwordx4 v[216:217], v[210:213], off offset:2048
	s_andn2_b64 vcc, exec, s[2:3]
	s_cbranch_vccnz .LBB0_242
	s_andn2_b64 vcc, exec, s[4:5]
	s_cbranch_vccnz .LBB0_241
	s_branch .LBB0_241
